# attention stream's bf16 row stores issued system-scope non-temporal (sc0 sc1 nt) instead of nt
# speedup vs baseline: 1.0152x; 1.0011x over previous
; #define LAS __attribute__((address_space(3)))
; __device__ __forceinline__ unsigned pk2(float lo, float hi) { return f2bf(lo) | (f2bf(hi) << 16); }
;     __device__ __forceinline__ const float* x() const { return (const float*)ld(0); }
;     __device__ __forceinline__ const float* c() const { return (const float*)ld(1); }
; template <bool NT = true> __device__ __forceinline__ void cvt_store(const CvtItem& d, const f32x4 (&v)[8], LAS float* scr, int lane) {
;     const int rr = lane >> 3, c4 = (lane & 7) * 4;
; #pragma unroll
;     for (int q = 0; q < 8; ++q) { LAS float* t = scr + (8 * q + rr) * 33 + c4; t[0] = v[q].x; t[1] = v[q].y; t[2] = v[q].z; t[3] = v[q].w; }
;     asm volatile("s_waitcnt lgkmcnt(0)" ::: "memory");
;     const int c = lane & 7;
; #pragma unroll
;     for (int j = 0; j < 4; ++j) { const int n = (lane >> 3) + 8 * j; const LAS float* s = scr + (8 * c) * 33 + n;
;         u32x4 o; o.x = pk2(s[0 * 33], s[1 * 33]); o.y = pk2(s[2 * 33], s[3 * 33]); o.z = pk2(s[4 * 33], s[5 * 33]); o.w = pk2(s[6 * 33], s[7 * 33]);
;         const int ng = d.n0 + n, drow = d.row_off + (d.ilv ? ((ng >> 7) * 256 + (ng & 127)) : ng);
;         if (NT) __builtin_nontemporal_store(o, (u32x4*)(d.dst + (size_t)drow * d.K + d.k0 + 8 * c)); else *(u32x4*)(d.dst + (size_t)drow * d.K + d.k0 + 8 * c) = o; }
.LBB0_529:
	v_mfma_f32_32x32x16_bf16 v[66:81], v[194:197], v[134:137], v[66:81]
	v_exp_f32_e32 v162, v162
	v_exp_f32_e32 v163, v163
	ds_read_b64_tr_b16 v[122:123], v16 offset:50176
	ds_read_b64_tr_b16 v[124:125], v16 offset:50688
	s_add_u32 s58, s33, 0xfef80000
	s_addc_u32 s59, s53, -1
	s_add_u32 s2, s33, 0xfefe0000
	s_addc_u32 s3, s53, -1
	s_add_i32 s60, s57, s49
	s_mov_b32 s61, m0
	s_mov_b32 m0, s60
	s_nop 0
	global_load_lds_dwordx4 v237, s[2:3] offset:0
	s_mov_b32 m0, s61
	v_mfma_f32_32x32x16_bf16 v[82:97], v[194:197], v[130:133], v[82:97]
	v_exp_f32_e32 v164, v164
	v_exp_f32_e32 v165, v165
	ds_read_b64_tr_b16 v[126:127], v16 offset:54272
	ds_read_b64_tr_b16 v[128:129], v16 offset:54784
	s_waitcnt lgkmcnt(6)
	v_mfma_f32_32x32x16_bf16 v[34:49], v[194:197], v[118:121], v[34:49]
	v_exp_f32_e32 v166, v166
	v_exp_f32_e32 v167, v167
	ds_read_b64_tr_b16 v[130:131], v16 offset:58368
	ds_read_b64_tr_b16 v[132:133], v16 offset:58880
	s_add_u32 s2, s33, 0xfefe0080
	s_addc_u32 s3, s53, -1
	s_add_i32 s60, s57, s54
	s_mov_b32 s61, m0
	s_mov_b32 m0, s60
	s_nop 0
	global_load_lds_dwordx4 v237, s[2:3] offset:0
	s_mov_b32 m0, s61
	s_waitcnt lgkmcnt(6)
	v_mfma_f32_32x32x16_bf16 v[50:65], v[194:197], v[114:117], v[50:65]
	v_exp_f32_e32 v168, v168
	v_exp_f32_e32 v169, v169
	ds_read_b64_tr_b16 v[118:119], v16 offset:62464
	ds_read_b64_tr_b16 v[120:121], v16 offset:62976
	v_add_u32_e32 v17, s55, v236
	ds_read_b128 v[114:117], v17
	ds_read_b128 v[178:181], v17 offset:512
	s_waitcnt lgkmcnt(8)
	v_mfma_f32_32x32x16_bf16 v[66:81], v[12:15], v[122:125], v[66:81]
	v_exp_f32_e32 v170, v170
	v_exp_f32_e32 v171, v171
	ds_read_b64_tr_b16 v[134:135], v16 offset:51200
	ds_read_b64_tr_b16 v[136:137], v16 offset:51712
	s_add_u32 s2, s33, 0x20000
	s_addc_u32 s3, s53, 0
	s_add_i32 s60, s55, s46
	s_mov_b32 s61, m0
	s_mov_b32 m0, s60
	s_nop 0
	global_load_lds_dwordx4 v235, s[2:3] offset:0
	s_mov_b32 m0, s61
	s_waitcnt lgkmcnt(8)
	v_mfma_f32_32x32x16_bf16 v[82:97], v[12:15], v[126:129], v[82:97]
	v_exp_f32_e32 v172, v172
	v_exp_f32_e32 v173, v173
	ds_read_b64_tr_b16 v[122:123], v16 offset:55296
	ds_read_b64_tr_b16 v[124:125], v16 offset:55808
	ds_read_b128 v[198:201], v17 offset:2048
	ds_read_b128 v[186:189], v17 offset:2560
	s_waitcnt lgkmcnt(10)
	v_mfma_f32_32x32x16_bf16 v[34:49], v[12:15], v[130:133], v[34:49]
	v_exp_f32_e32 v174, v174
	v_exp_f32_e32 v175, v175
	ds_read_b64_tr_b16 v[126:127], v16 offset:59392
	ds_read_b64_tr_b16 v[128:129], v16 offset:59904
	s_add_u32 s2, s33, 0x20080
	s_addc_u32 s3, s53, 0
	s_add_i32 s60, s55, s45
	s_mov_b32 s61, m0
	s_mov_b32 m0, s60
	s_nop 0
	global_load_lds_dwordx4 v235, s[2:3] offset:0
	s_mov_b32 m0, s61
	s_waitcnt lgkmcnt(10)
	v_mfma_f32_32x32x16_bf16 v[50:65], v[12:15], v[118:121], v[50:65]
	v_exp_f32_e32 v176, v176
	v_exp_f32_e32 v177, v177
	ds_read_b64_tr_b16 v[130:131], v16 offset:63488
	ds_read_b64_tr_b16 v[132:133], v16 offset:64000
	ds_read_b128 v[206:209], v17 offset:4096
	ds_read_b128 v[190:193], v17 offset:4608
	s_waitcnt lgkmcnt(10)
	v_mfma_f32_32x32x16_bf16 v[66:81], v[8:11], v[134:137], v[66:81]
	v_exp_f32_e32 v146, v146
	v_exp_f32_e32 v147, v147
	ds_read_b64_tr_b16 v[118:119], v16 offset:52224
	ds_read_b64_tr_b16 v[120:121], v16 offset:52736
	s_waitcnt lgkmcnt(10)
	v_mfma_f32_32x32x16_bf16 v[82:97], v[8:11], v[122:125], v[82:97]
	v_exp_f32_e32 v148, v148
	v_exp_f32_e32 v149, v149
	ds_read_b64_tr_b16 v[134:135], v16 offset:56320
	ds_read_b64_tr_b16 v[136:137], v16 offset:56832
	ds_read_b128 v[202:205], v17 offset:6144
	ds_read_b128 v[182:185], v17 offset:6656
	s_waitcnt lgkmcnt(10)
	v_mfma_f32_32x32x16_bf16 v[34:49], v[8:11], v[126:129], v[34:49]
	v_exp_f32_e32 v150, v150
	v_exp_f32_e32 v151, v151
	ds_read_b64_tr_b16 v[122:123], v16 offset:60416
	ds_read_b64_tr_b16 v[124:125], v16 offset:60928
	s_waitcnt lgkmcnt(10)
	v_mfma_f32_32x32x16_bf16 v[50:65], v[8:11], v[130:133], v[50:65]
	v_exp_f32_e32 v152, v152
	v_exp_f32_e32 v153, v153
	ds_read_b64_tr_b16 v[126:127], v16 offset:64512
	ds_read_b64_tr_b16 v[128:129], v16 offset:65024
	s_waitcnt lgkmcnt(8)
	v_mfma_f32_32x32x16_bf16 v[66:81], v[4:7], v[118:121], v[66:81]
	v_exp_f32_e32 v154, v154
	v_exp_f32_e32 v155, v155
	s_waitcnt lgkmcnt(6)
	v_mfma_f32_32x32x16_bf16 v[82:97], v[4:7], v[134:137], v[82:97]
	v_exp_f32_e32 v156, v156
	v_exp_f32_e32 v157, v157
	s_waitcnt lgkmcnt(2)
	v_mfma_f32_32x32x16_bf16 v[34:49], v[4:7], v[122:125], v[34:49]
	v_exp_f32_e32 v158, v158
	v_exp_f32_e32 v159, v159
	s_add_i32 s2, s56, 1
	s_cmp_gt_i32 s2, s90
	s_cbranch_scc1 .Lcs_done_h0
	s_waitcnt vmcnt(6)
	v_cvt_pk_bf16_f32 v245, v250, v251
	v_cvt_pk_bf16_f32 v244, v252, v253
	s_cmp_lt_u32 s2, 7
	s_cbranch_scc1 .Lcs_dumS_h0
	s_bitcmp1_b32 s2, 1
	s_cbranch_scc1 .Lcs_Sb_h0
	global_store_dwordx2 v28, v[30:31], s[100:101] sc0 sc1 nt
	v_add_u32_e32 v28, s63, v28

; #define LAS __attribute__((address_space(3)))
; __device__ __forceinline__ unsigned pk2(float lo, float hi) { return f2bf(lo) | (f2bf(hi) << 16); }
;     __device__ __forceinline__ const float* x() const { return (const float*)ld(0); }
;     __device__ __forceinline__ const float* c() const { return (const float*)ld(1); }
; template <bool NT = true> __device__ __forceinline__ void cvt_store(const CvtItem& d, const f32x4 (&v)[8], LAS float* scr, int lane) {
;     ...
;     for (int j = 0; j < 4; ++j) { const int n = (lane >> 3) + 8 * j; const LAS float* s = scr + (8 * c) * 33 + n;
;         u32x4 o; o.x = pk2(s[0 * 33], s[1 * 33]); o.y = pk2(s[2 * 33], s[3 * 33]); o.z = pk2(s[4 * 33], s[5 * 33]); o.w = pk2(s[6 * 33], s[7 * 33]);
;         const int ng = d.n0 + n, drow = d.row_off + (d.ilv ? ((ng >> 7) * 256 + (ng & 127)) : ng);
;         if (NT) __builtin_nontemporal_store(o, (u32x4*)(d.dst + (size_t)drow * d.K + d.k0 + 8 * c)); else *(u32x4*)(d.dst + (size_t)drow * d.K + d.k0 + 8 * c) = o; }
.Lcs_Sgo_h1:
	s_bitcmp1_b32 s2, 1
	s_cbranch_scc1 .Lcs_Sb_h1
	global_store_dwordx2 v28, v[22:23], s[100:101] sc0 sc1 nt
	v_add_u32_e32 v28, s63, v28

; #define LAS __attribute__((address_space(3)))
; __device__ __forceinline__ unsigned pk2(float lo, float hi) { return f2bf(lo) | (f2bf(hi) << 16); }
;     __device__ __forceinline__ const float* x() const { return (const float*)ld(0); }
;     __device__ __forceinline__ const float* c() const { return (const float*)ld(1); }
; template <bool NT = true> __device__ __forceinline__ void cvt_store(const CvtItem& d, const f32x4 (&v)[8], LAS float* scr, int lane) {
;     ...
;     for (int j = 0; j < 4; ++j) { const int n = (lane >> 3) + 8 * j; const LAS float* s = scr + (8 * c) * 33 + n;
;         u32x4 o; o.x = pk2(s[0 * 33], s[1 * 33]); o.y = pk2(s[2 * 33], s[3 * 33]); o.z = pk2(s[4 * 33], s[5 * 33]); o.w = pk2(s[6 * 33], s[7 * 33]);
;         const int ng = d.n0 + n, drow = d.row_off + (d.ilv ? ((ng >> 7) * 256 + (ng & 127)) : ng);
;         if (NT) __builtin_nontemporal_store(o, (u32x4*)(d.dst + (size_t)drow * d.K + d.k0 + 8 * c)); else *(u32x4*)(d.dst + (size_t)drow * d.K + d.k0 + 8 * c) = o; }
.Lcs_Sb_h0:
	global_store_dwordx2 v28, v[26:27], s[100:101] sc0 sc1 nt
	v_subrev_u32_e32 v28, s87, v28
	s_branch .Lcs_noS_h0

; #define LAS __attribute__((address_space(3)))
; __device__ __forceinline__ unsigned pk2(float lo, float hi) { return f2bf(lo) | (f2bf(hi) << 16); }
;     __device__ __forceinline__ const float* x() const { return (const float*)ld(0); }
;     __device__ __forceinline__ const float* c() const { return (const float*)ld(1); }
; template <bool NT = true> __device__ __forceinline__ void cvt_store(const CvtItem& d, const f32x4 (&v)[8], LAS float* scr, int lane) {
;     ...
;     for (int j = 0; j < 4; ++j) { const int n = (lane >> 3) + 8 * j; const LAS float* s = scr + (8 * c) * 33 + n;
;         u32x4 o; o.x = pk2(s[0 * 33], s[1 * 33]); o.y = pk2(s[2 * 33], s[3 * 33]); o.z = pk2(s[4 * 33], s[5 * 33]); o.w = pk2(s[6 * 33], s[7 * 33]);
;         const int ng = d.n0 + n, drow = d.row_off + (d.ilv ? ((ng >> 7) * 256 + (ng & 127)) : ng);
;         if (NT) __builtin_nontemporal_store(o, (u32x4*)(d.dst + (size_t)drow * d.K + d.k0 + 8 * c)); else *(u32x4*)(d.dst + (size_t)drow * d.K + d.k0 + 8 * c) = o; }
.Lcs_Sb_h1:
	global_store_dwordx2 v28, v[254:255], s[100:101] sc0 sc1 nt
	v_add_u32_e32 v28, s63, v28
	s_branch .Lcs_noS_h1
